# c3_coop2
# speedup vs baseline: 1.0084x; 1.0009x over previous
.LBB3_3:
	v_lshrrev_b32_e32 v2, 2, v0
	v_sub_u32_e32 v2, 0, v2
	s_lshr_b32 s9, s5, 2
	s_load_dwordx2 s[2:3], s[0:1], 0x30
	s_load_dwordx2 s[14:15], s[0:1], 0x8
	s_load_dwordx2 s[18:19], s[0:1], 0x0
	v_and_b32_e32 v34, 15, v0
	v_bitop3_b32 v2, v1, v2, 3 bitop3:0x78
	s_and_b32 s9, s9, 64
	s_lshl_b32 s10, s6, 5
	v_lshlrev_b32_e32 v35, 4, v2
	v_or_b32_e32 v2, s9, v34
	s_and_b32 s10, s10, 0x60
	v_lshlrev_b32_e32 v36, 6, v2
	v_or_b32_e32 v2, s10, v34
	v_lshlrev_b32_e32 v37, 6, v2
	v_mov_b32_e32 v2, 0
	s_mov_b32 s8, 0
	s_mov_b32 s11, 32
	v_mov_b32_e32 v3, v2
	v_mov_b32_e32 v4, v2
	v_mov_b32_e32 v5, v2
	v_mov_b32_e32 v10, v2
	v_mov_b32_e32 v11, v2
	v_mov_b32_e32 v12, v2
	v_mov_b32_e32 v13, v2
	v_mov_b32_e32 v6, v2
	v_mov_b32_e32 v7, v2
	v_mov_b32_e32 v8, v2
	v_mov_b32_e32 v9, v2
	v_mov_b32_e32 v18, v2
	v_mov_b32_e32 v19, v2
	v_mov_b32_e32 v20, v2
	v_mov_b32_e32 v21, v2
	v_mov_b32_e32 v14, v2
	v_mov_b32_e32 v15, v2
	v_mov_b32_e32 v16, v2
	v_mov_b32_e32 v17, v2
	v_mov_b32_e32 v26, v2
	v_mov_b32_e32 v27, v2
	v_mov_b32_e32 v28, v2
	v_mov_b32_e32 v29, v2
	v_mov_b32_e32 v22, v2
	v_mov_b32_e32 v23, v2
	v_mov_b32_e32 v24, v2
	v_mov_b32_e32 v25, v2
	v_mov_b32_e32 v30, v2
	v_mov_b32_e32 v31, v2
	v_mov_b32_e32 v32, v2
	v_mov_b32_e32 v33, v2
	v_and_b32_e32 v62, 63, v0
	v_lshrrev_b32_e32 v63, 2, v62
	v_and_b32_e32 v62, 3, v62
	v_sub_u32_e32 v64, 0, v1
	v_and_b32_e32 v64, 3, v64
	v_xor_b32_e32 v62, v62, v64
	v_lshlrev_b32_e32 v62, 4, v62
	v_lshl_or_b32 v62, v63, 11, v62
	s_lshl_b32 s13, s6, 4
	s_add_i32 s13, s13, s4
	s_lshl_b32 s13, s13, 11
	s_lshl_b32 s16, s6, 10
	s_add_i32 s16, s16, 0x2000
	s_waitcnt lgkmcnt(0)
	s_add_u32 s14, s14, s13
	s_addc_u32 s15, s15, 0
	s_lshl_b32 s13, s6, 4
	s_add_i32 s13, s13, s7
	s_lshl_b32 s13, s13, 11
	s_add_u32 s18, s18, s13
	s_addc_u32 s19, s19, 0
	s_lshl_b32 s20, s6, 10
	s_add_i32 m0, s16, 0
	s_nop 0
	global_load_lds_dwordx4 v62, s[14:15] offset:0
	s_add_i32 m0, s20, 0
	s_nop 0
	global_load_lds_dwordx4 v62, s[18:19] offset:0
	s_add_i32 m0, s16, 16320
	s_nop 0
	global_load_lds_dwordx4 v62, s[14:15] offset:64
	s_add_i32 m0, s20, 16320
	s_nop 0
	global_load_lds_dwordx4 v62, s[18:19] offset:64
	s_add_i32 m0, s16, 32640
	s_nop 0
	global_load_lds_dwordx4 v62, s[14:15] offset:128
	s_add_i32 m0, s20, 32640
	s_nop 0
	global_load_lds_dwordx4 v62, s[18:19] offset:128
	s_add_i32 m0, s16, 48960
	s_nop 0
	global_load_lds_dwordx4 v62, s[14:15] offset:192
	s_add_i32 m0, s20, 48960
	s_nop 0
	global_load_lds_dwordx4 v62, s[18:19] offset:192
	v_add_u32_e32 v62, 0x100, v62
	s_mov_b32 s17, 4
.Lg1_cloop:
	s_lshl_b32 s12, s8, 14
	v_add3_u32 v42, s12, v37, v35
	v_add3_u32 v58, s12, v36, v35
	s_waitcnt vmcnt(6)
	s_barrier
	ds_read_b128 v[38:41], v42 offset:8192
	ds_read_b128 v[42:45], v42 offset:9216
	ds_read_b128 v[46:49], v58
	ds_read_b128 v[50:53], v58 offset:1024
	ds_read_b128 v[54:57], v58 offset:2048
	ds_read_b128 v[58:61], v58 offset:3072
	s_lshl_b32 s13, s17, 14
	s_add_i32 m0, s13, s16
	s_add_i32 s21, s13, s20
	global_load_lds_dwordx4 v62, s[14:15]
	s_mov_b32 m0, s21
	s_add_i32 s13, s17, 1
	global_load_lds_dwordx4 v62, s[18:19]
	s_cmp_lg_u32 s17, 4
	s_cselect_b32 s17, s13, 0
	v_add_u32_e32 v62, 64, v62
	s_waitcnt lgkmcnt(0)
	v_mfma_f32_16x16x32_f16 v[30:33], v[46:49], v[38:41], v[30:33]
	s_add_i32 s12, s8, 1
	s_cmp_lg_u32 s8, 4
	s_cselect_b32 s8, s12, 0
	v_mfma_f32_16x16x32_f16 v[22:25], v[46:49], v[42:45], v[22:25]
	s_add_i32 s11, s11, -1
	s_cmp_eq_u32 s11, 0
	v_mfma_f32_16x16x32_f16 v[26:29], v[50:53], v[38:41], v[26:29]
	v_mfma_f32_16x16x32_f16 v[14:17], v[50:53], v[42:45], v[14:17]
	v_mfma_f32_16x16x32_f16 v[18:21], v[54:57], v[38:41], v[18:21]
	v_mfma_f32_16x16x32_f16 v[6:9], v[54:57], v[42:45], v[6:9]
	v_mfma_f32_16x16x32_f16 v[10:13], v[58:61], v[38:41], v[10:13]
	v_mfma_f32_16x16x32_f16 v[2:5], v[58:61], v[42:45], v[2:5]
	s_cbranch_scc0 .Lg1_cloop
	s_or_b32 s8, s10, s4
	v_or_b32_e32 v35, s8, v34
	v_lshl_or_b32 v34, v1, 2, s9
	v_mov_b32_e32 v37, 0
	v_or_b32_e32 v34, s7, v34
	v_lshlrev_b32_e32 v36, 12, v35
	v_mov_b32_e32 v35, v37
	v_lshl_add_u64 v[38:39], s[2:3], 0, v[36:37]
	v_lshlrev_b64 v[40:41], 2, v[34:35]
	v_lshl_add_u64 v[42:43], v[38:39], 0, v[40:41]
	s_mov_b64 s[2:3], 0x10000
	v_lshl_add_u64 v[44:45], v[42:43], 0, s[2:3]
	global_store_dwordx4 v[42:43], v[30:33], off sc1
	global_store_dwordx4 v[42:43], v[26:29], off offset:64 sc1
	global_store_dwordx4 v[42:43], v[18:21], off offset:128 sc1
	global_store_dwordx4 v[42:43], v[10:13], off offset:192 sc1
	global_store_dwordx4 v[44:45], v[22:25], off sc1
	global_store_dwordx4 v[44:45], v[14:17], off offset:64 sc1
	global_store_dwordx4 v[44:45], v[6:9], off offset:128 sc1
	global_store_dwordx4 v[44:45], v[2:5], off offset:192 sc1
	s_branch .LBB3_2
.LBB3_6:
	s_mov_b32 s0, 32
.Lg1_pb:
	s_barrier
	s_add_i32 s0, s0, -1
	s_cmp_eq_u32 s0, 0
	s_cbranch_scc0 .Lg1_pb
	s_endpgm
